# baseline (speedup 1.0000x reference)
_Z11jacobi_mainPKfS0_S0_PyPf:
	s_lshl_b32 s3, s2, 3
	s_load_dwordx4 s[12:15], s[0:1], 0x0
	s_load_dwordx2 s[4:5], s[0:1], 0x10
	s_getpc_b64 s[88:89]
	v_lshlrev_b32_e32 v250, 6, v0
	v_and_b32_e32 v250, 0xfc0, v250
	v_mov_b32_e32 v251, 0
	s_add_u32 s90, s88, 0x000067c0
	s_addc_u32 s91, s89, 0
	v_lshl_add_u64 v[252:253], s[90:91], 0, v[250:251]
	global_load_dword v248, v[252:253], off
	v_min_u32_e32 v250, 0x4c0, v250
	v_add_u32_e32 v250, 0x1000, v250
	v_lshl_add_u64 v[252:253], s[90:91], 0, v[250:251]
	global_load_dword v249, v[252:253], off
	s_and_b32 s3, s3, 56
	s_ashr_i32 s33, s2, 5
	v_readfirstlane_b32 s40, v0
	s_add_i32 s18, s3, s33
	s_bfe_u32 s3, s2, 0x20003
	s_lshl_b32 s7, s3, 8
	s_and_b32 s10, s40, 0xffffffc0
	s_ashr_i32 s19, s18, 31
	s_lshr_b32 s34, s2, 3
	s_add_i32 s11, s10, s7
	s_lshl_b64 s[8:9], s[18:19], 22
	v_and_b32_e32 v206, 63, v0
	s_waitcnt lgkmcnt(0)
	s_add_u32 s8, s12, s8
	s_addc_u32 s9, s13, s9
	v_or_b32_e32 v154, s11, v206
	s_lshl_b32 s6, s18, 10
	v_add_u32_e32 v2, s6, v154
	v_ashrrev_i32_e32 v3, 31, v2
	v_lshlrev_b64 v[2:3], 2, v[2:3]
	v_lshl_add_u64 v[4:5], s[14:15], 0, v[2:3]
	global_load_dword v1, v[4:5], off
	s_movk_i32 s12, 0x1004
	v_mov_b64_e32 v[4:5], s[8:9]
	v_mad_i64_i32 v[4:5], s[12:13], v154, s12, v[4:5]
	v_lshl_add_u64 v[2:3], s[4:5], 0, v[2:3]
	global_load_dword v207, v[4:5], off
	global_load_dword v66, v[2:3], off
	s_lshl_b32 s76, s6, 2
	s_add_u32 s76, s4, s76
	s_addc_u32 s77, s5, 0
	v_lshlrev_b32_e32 v220, 4, v0
	global_load_dwordx4 v[224:227], v220, s[76:77]
	s_load_dwordx2 s[16:17], s[0:1], 0x20
	v_ashrrev_i32_e32 v155, 31, v154
	s_mov_b32 s21, 0
	s_lshr_b32 s35, s40, 6
	v_cmp_eq_u32_e64 s[12:13], 0, v206
	s_load_dwordx2 s[0:1], s[0:1], 0x18
	v_lshrrev_b32_e32 v67, 5, v206
	v_or_b32_e32 v132, s11, v67
	s_lshl_b64 s[14:15], s[18:19], 14
	v_ashrrev_i32_e32 v133, 31, v132
	v_and_b32_e32 v124, 31, v0
	s_waitcnt lgkmcnt(0)
	s_add_u32 s14, s0, s14
	v_lshlrev_b64 v[2:3], 12, v[132:133]
	s_addc_u32 s15, s1, s15
	s_add_i32 s0, s7, 0x100
	v_lshl_add_u64 v[2:3], s[8:9], 0, v[2:3]
	v_lshlrev_b32_e32 v190, 4, v124
	v_mov_b32_e32 v191, 0
	s_and_b32 s26, s0, 0x300
	v_lshl_add_u64 v[130:131], v[2:3], 0, v[190:191]
	s_mov_b64 s[0:1], 0x30000
	v_lshl_add_u64 v[126:127], v[130:131], 0, s[0:1]
	s_mov_b64 s[0:1], 0x32000
	v_lshl_add_u64 v[128:129], v[130:131], 0, s[0:1]
	s_mov_b64 s[0:1], 0x34000
	v_lshl_add_u64 v[134:135], v[130:131], 0, s[0:1]
	s_mov_b64 s[0:1], 0x36000
	v_lshl_add_u64 v[136:137], v[130:131], 0, s[0:1]
	s_mov_b64 s[0:1], 0x38000
	v_lshl_add_u64 v[138:139], v[130:131], 0, s[0:1]
	s_mov_b64 s[0:1], 0x3a000
	v_lshl_add_u64 v[140:141], v[130:131], 0, s[0:1]
	s_mov_b64 s[0:1], 0x3c000
	s_or_b32 s24, s7, 0x80
	v_lshl_add_u64 v[142:143], v[130:131], 0, s[0:1]
	s_mov_b64 s[0:1], 0x3e000
	s_lshl_b32 s20, s7, 2
	v_lshl_add_u64 v[144:145], v[130:131], 0, s[0:1]
	s_lshl_b32 s8, s24, 2
	s_mov_b32 s9, s21
	v_lshl_add_u64 v[2:3], v[126:127], 0, s[20:21]
	v_lshl_add_u64 v[4:5], v[128:129], 0, s[20:21]
	v_lshl_add_u64 v[6:7], v[134:135], 0, s[20:21]
	v_lshl_add_u64 v[8:9], v[136:137], 0, s[20:21]
	v_lshl_add_u64 v[10:11], v[138:139], 0, s[20:21]
	v_lshl_add_u64 v[12:13], v[140:141], 0, s[20:21]
	v_lshl_add_u64 v[14:15], v[142:143], 0, s[20:21]
	v_lshl_add_u64 v[16:17], v[144:145], 0, s[20:21]
	v_lshl_add_u64 v[18:19], v[126:127], 0, s[8:9]
	v_lshl_add_u64 v[20:21], v[128:129], 0, s[8:9]
	v_lshl_add_u64 v[22:23], v[134:135], 0, s[8:9]
	v_lshl_add_u64 v[24:25], v[136:137], 0, s[8:9]
	s_lshl_b32 s0, s26, 2
	s_mov_b32 s1, s21
	v_lshl_add_u64 v[72:73], v[138:139], 0, s[8:9]
	v_lshl_add_u64 v[102:103], v[140:141], 0, s[8:9]
	v_lshl_add_u64 v[104:105], v[142:143], 0, s[8:9]
	v_lshl_add_u64 v[106:107], v[144:145], 0, s[8:9]
	v_lshl_add_u64 v[108:109], v[126:127], 0, s[0:1]
	v_lshl_add_u64 v[110:111], v[128:129], 0, s[0:1]
	v_lshl_add_u64 v[112:113], v[134:135], 0, s[0:1]
	v_lshl_add_u64 v[114:115], v[136:137], 0, s[0:1]
	v_lshl_add_u64 v[116:117], v[138:139], 0, s[0:1]
	v_lshl_add_u64 v[118:119], v[140:141], 0, s[0:1]
	v_lshl_add_u64 v[120:121], v[142:143], 0, s[0:1]
	v_lshl_add_u64 v[122:123], v[144:145], 0, s[0:1]
	global_load_dwordx4 v[68:71], v[2:3], off nt
	global_load_dwordx4 v[78:81], v[4:5], off nt
	global_load_dwordx4 v[82:85], v[6:7], off nt
	global_load_dwordx4 v[90:93], v[8:9], off nt
	global_load_dwordx4 v[98:101], v[10:11], off nt
	global_load_dwordx4 v[62:65], v[12:13], off nt
	global_load_dwordx4 v[54:57], v[14:15], off nt
	global_load_dwordx4 v[46:49], v[16:17], off nt
	global_load_dwordx4 v[94:97], v[18:19], off nt
	global_load_dwordx4 v[86:89], v[20:21], off nt
	global_load_dwordx4 v[74:77], v[22:23], off nt
	global_load_dwordx4 v[58:61], v[24:25], off nt
	global_load_dwordx4 v[50:53], v[72:73], off nt
	global_load_dwordx4 v[42:45], v[102:103], off nt
	global_load_dwordx4 v[38:41], v[104:105], off nt
	global_load_dwordx4 v[34:37], v[106:107], off nt
	global_load_dwordx4 v[30:33], v[108:109], off nt
	global_load_dwordx4 v[26:29], v[110:111], off nt
	s_nop 0
	global_load_dwordx4 v[22:25], v[112:113], off nt
	global_load_dwordx4 v[18:21], v[114:115], off nt
	global_load_dwordx4 v[14:17], v[116:117], off nt
	global_load_dwordx4 v[10:13], v[118:119], off nt
	global_load_dwordx4 v[6:9], v[120:121], off nt
	global_load_dwordx4 v[2:5], v[122:123], off nt
	s_waitcnt vmcnt(25)
	v_div_scale_f32 v72, s[22:23], v207, v207, 1.0
	v_rcp_f32_e32 v73, v72
	s_lshl_b32 s11, s10, 2
	s_mul_i32 s19, s35, 0x1100
	s_add_i32 s22, s11, 0x26600
	v_fma_f32 v103, -v72, v73, 1.0
	v_fmac_f32_e32 v73, v103, v73
	v_div_scale_f32 v103, vcc, 1.0, v207, 1.0
	v_mul_f32_e32 v104, v103, v73
	v_fma_f32 v105, -v72, v104, v103
	v_fmac_f32_e32 v104, v105, v73
	v_fma_f32 v72, -v72, v104, v103
	v_div_fmas_f32 v72, v72, v73, v104
	v_div_fixup_f32 v72, v72, v207, 1.0
	s_waitcnt vmcnt(24)
	v_fma_f32 v208, v72, v1, -v66
	v_mbcnt_lo_u32_b32 v244, -1, 0
	v_mbcnt_hi_u32_b32 v244, -1, v244
	v_and_b32_e32 v245, 64, v244
	v_xor_b32_e32 v246, 32, v244
	v_add_u32_e32 v245, 64, v245
	v_cmp_lt_i32_e32 vcc, v246, v245
	v_xor_b32_e32 v248, 8, v244
	s_nop 0
	v_cndmask_b32_e32 v246, v244, v246, vcc
	v_lshlrev_b32_e32 v246, 2, v246
	v_mul_f32_e32 v247, v1, v1
	ds_bpermute_b32 v246, v246, v247
	v_xor_b32_e32 v247, 16, v244
	v_cmp_lt_i32_e32 vcc, v247, v245
	s_waitcnt lgkmcnt(0)
	v_fmac_f32_e32 v246, v1, v1
	v_cndmask_b32_e32 v247, v244, v247, vcc
	v_lshlrev_b32_e32 v247, 2, v247
	ds_bpermute_b32 v247, v247, v246
	v_cmp_lt_i32_e32 vcc, v248, v245
	s_waitcnt lgkmcnt(0)
	v_add_f32_e32 v246, v246, v247
	v_cndmask_b32_e32 v248, v244, v248, vcc
	v_lshlrev_b32_e32 v248, 2, v248
	ds_bpermute_b32 v247, v248, v246
	v_xor_b32_e32 v248, 4, v244
	v_cmp_lt_i32_e32 vcc, v248, v245
	s_waitcnt lgkmcnt(0)
	v_add_f32_e32 v246, v246, v247
	v_cndmask_b32_e32 v248, v244, v248, vcc
	v_lshlrev_b32_e32 v248, 2, v248
	ds_bpermute_b32 v247, v248, v246
	v_xor_b32_e32 v248, 2, v244
	v_cmp_lt_i32_e32 vcc, v248, v245
	s_waitcnt lgkmcnt(0)
	v_add_f32_e32 v246, v246, v247
	v_cndmask_b32_e32 v248, v244, v248, vcc
	v_lshlrev_b32_e32 v248, 2, v248
	ds_bpermute_b32 v247, v248, v246
	v_xor_b32_e32 v248, 1, v244
	v_cmp_lt_i32_e32 vcc, v248, v245
	s_nop 1
	v_cndmask_b32_e32 v245, v244, v248, vcc
	s_waitcnt lgkmcnt(0)
	v_add_f32_e32 v244, v246, v247
	v_lshlrev_b32_e32 v245, 2, v245
	ds_bpermute_b32 v245, v245, v244
	s_and_saveexec_b64 s[80:81], s[12:13]
	s_cbranch_execz .LBB0_2
	s_lshl_b32 s82, s35, 2
	s_add_i32 s82, s82, 0x26a00
	s_waitcnt lgkmcnt(0)
	v_add_f32_e32 v244, v244, v245
	v_mov_b32_e32 v245, s82
	ds_write_b32 v245, v244
